# BN stats accumulated into 2 copies (even/odd WG) to halve same-line atomic contention; consumers sum both copies
# speedup vs baseline: 1.0572x; 1.0185x over previous
.LBB0_6:
	v_mbcnt_lo_u32_b32 v3, -1, 0
	v_mbcnt_hi_u32_b32 v3, -1, v3
	s_lshr_b32 s12, s2, 3
	s_mov_b32 s13, 0
	v_and_b32_e32 v5, 64, v3
	s_and_b32 s3, s2, 7
	s_lshl_b64 s[0:1], s[12:13], 20
	v_xor_b32_e32 v4, 16, v3
	v_add_u32_e32 v5, 64, v5
	s_waitcnt lgkmcnt(0)
	s_add_u32 s8, s4, s0
	v_cmp_lt_i32_e32 vcc, v4, v5
	v_lshrrev_b32_e32 v62, 6, v0
	s_addc_u32 s0, s5, s1
	s_lshl_b32 s12, s12, 9
	v_cndmask_b32_e32 v4, v3, v4, vcc
	s_and_b32 s9, s0, 0xffff
	v_lshlrev_b32_e32 v2, 2, v62
	v_lshlrev_b32_e32 v65, 2, v4
	v_xor_b32_e32 v4, 32, v3
	s_lshl_b64 s[4:5], s[12:13], 2
	v_and_b32_e32 v1, 63, v0
	v_cmp_lt_i32_e32 vcc, v4, v5
	v_lshl_add_u32 v66, s3, 6, v2
	s_add_u32 s4, s6, s4
	v_lshlrev_b32_e32 v2, 13, v62
	v_lshlrev_b32_e32 v63, 4, v1
	v_cndmask_b32_e32 v3, v3, v4, vcc
	v_lshlrev_b32_e32 v42, 2, v66
	v_mov_b32_e32 v43, 0
	s_addc_u32 s5, s7, s5
	v_lshl_add_u32 v2, s3, 17, v2
	s_mov_b32 s11, 0x20000
	s_mov_b32 s10, 0x100000
	v_lshlrev_b32_e32 v64, 2, v3
	v_cmp_eq_u32_e64 s[0:1], 0, v1
	v_lshl_add_u64 v[44:45], s[4:5], 0, v[42:43]
	v_lshrrev_b32_e32 v67, 2, v66
	v_or_b32_e32 v68, v2, v63
	v_mov_b32_e32 v42, v43
	v_mov_b32_e32 v2, v43
	v_mov_b32_e32 v3, v43
	v_mov_b32_e32 v4, v43
	v_mov_b32_e32 v5, v43
	v_mov_b32_e32 v6, v43
	v_mov_b32_e32 v7, v43
	v_mov_b32_e32 v8, v43
	v_mov_b32_e32 v9, v43
	s_sub_u32 s14, s2, 64
	s_cmp_lt_u32 s14, 6
	s_cbranch_scc0 .Lk1_nozero
	v_lshlrev_b32_e32 v10, 4, v0
	s_lshl_b32 s14, s14, 12
	v_add_u32_e32 v10, s14, v10
	v_add_u32_e32 v10, 0x582000, v10
	global_store_dwordx4 v10, v[2:5], s[6:7]

_Z9k2_layer1PKfS0_S0_PfS1_S1_:
	s_load_dwordx8 s[4:11], s[0:1], 0x0
	s_load_dwordx4 s[12:15], s[0:1], 0x20
	s_lshr_b32 s16, s2, 5
	s_and_b32 s17, s2, 31
	s_lshl_b32 s17, s17, 4
	s_movk_i32 s18, 0x500
	v_and_b32_e32 v1, 15, v0
	v_lshrrev_b32_e32 v2, 4, v0
	v_lshl_add_u32 v3, s16, 4, v2
	v_add_u32_e32 v4, s17, v1
	v_lshlrev_b32_e32 v4, 2, v4
	v_lshl_add_u32 v5, v3, 11, v4
	v_add_u32_e32 v6, 0x40000, v5
	v_lshl_add_u32 v7, v3, 14, v4
	v_add_u32_e32 v7, 0x80000, v7
	v_add_u32_e32 v8, 0x1000, v7
	v_add_u32_e32 v9, 0x2000, v7
	v_add_u32_e32 v10, 0x3000, v7
	v_and_b32_e32 v11, 7, v1
	v_lshl_add_u32 v11, v3, 3, v11
	v_lshlrev_b32_e32 v11, 2, v11
	v_and_b32_e32 v12, 8, v1
	v_lshl_add_u32 v11, v12, 9, v11
	v_add_u32_e32 v11, 0x280000, v11
	v_lshrrev_b32_e32 v13, 6, v0
	v_bfe_u32 v14, v0, 4, 2
	v_lshl_add_u32 v15, v13, 4, v1
	v_mul_u32_u24_e32 v16, 20, v15
	v_mad_u32_u24 v16, v14, s18, v16
	v_add_u32_e32 v17, 0x1400, v16
	v_add_u32_e32 v18, 0x2800, v16
	v_add_u32_e32 v19, 0x3c00, v16
	v_lshlrev_b32_e32 v20, 2, v15
	s_waitcnt lgkmcnt(0)
	global_load_dword v24, v5, s[4:5]
	global_load_dword v25, v6, s[4:5]
	global_load_dword v26, v7, s[4:5]
	global_load_dword v27, v7, s[4:5] offset:2048
	global_load_dword v28, v8, s[4:5]
	global_load_dword v29, v8, s[4:5] offset:2048
	global_load_dword v30, v9, s[4:5]
	global_load_dword v31, v9, s[4:5] offset:2048
	global_load_dword v32, v10, s[4:5]
	global_load_dword v33, v10, s[4:5] offset:2048
	global_load_dword v34, v11, s[4:5]
	global_load_dwordx4 v[36:39], v16, s[6:7]
	global_load_dwordx4 v[40:43], v17, s[6:7]
	global_load_dwordx4 v[44:47], v18, s[6:7]
	global_load_dwordx4 v[48:51], v19, s[6:7]
	global_load_dword v52, v16, s[6:7] offset:16
	global_load_dword v53, v17, s[6:7] offset:16
	global_load_dword v54, v18, s[6:7] offset:16
	global_load_dword v55, v19, s[6:7] offset:16
	global_load_dword v56, v20, s[8:9]
	v_lshlrev_b32_e32 v21, 2, v0
	v_and_b32_e32 v22, 63, v0
	v_lshlrev_b32_e32 v22, 2, v22
	v_lshlrev_b32_e32 v23, 2, v14
	v_add_u32_e32 v23, 0xc00, v23
	v_lshlrev_b32_e32 v57, 3, v12
	v_lshl_add_u32 v57, v2, 2, v57
	v_add_u32_e32 v57, 0xc00, v57
	v_mul_u32_u24_e32 v58, 0x900000, v12
	v_sub_u32_e32 v58, 0x3b000000, v58
	s_lshl_b32 s19, s2, 4
	v_add_u32_e32 v59, s19, v1
	v_lshlrev_b32_e32 v59, 6, v59
	v_lshl_add_u32 v59, v13, 4, v59
	v_lshl_add_u32 v59, v14, 2, v59
	v_lshlrev_b32_e32 v59, 2, v59
	v_and_b32_e32 v90, 3, v1
	v_lshl_add_u32 v90, v14, 2, v90
	v_lshl_add_u32 v90, v13, 4, v90
	s_lshl_b32 s19, s16, 8
	s_and_b32 s20, s2, 1
	s_mul_i32 s20, s20, 0x3000
	s_add_u32 s19, s19, s20
	v_lshl_add_u32 v90, v90, 2, s19
	v_mov_b32_e32 v89, 1.0
	s_mov_b32 s20, 0x01010101
	s_mov_b32 s21, 0x01010101
	s_mov_b32 s22, 0xffff
	s_mov_b32 s23, 0
	s_waitcnt vmcnt(9)
	v_add_f32_dpp v34, v34, v34 quad_perm:[1,0,3,2] row_mask:0xf bank_mask:0xf
	v_add_f32_e32 v26, v26, v27
	v_add_f32_e32 v28, v28, v29
	v_add_f32_dpp v34, v34, v34 quad_perm:[2,3,0,1] row_mask:0xf bank_mask:0xf
	v_add_f32_e32 v30, v30, v31
	v_add_f32_e32 v32, v32, v33
	v_add_f32_dpp v34, v34, v34 row_half_mirror row_mask:0xf bank_mask:0xf
	v_add_f32_e32 v26, v26, v28
	v_add_f32_e32 v30, v30, v32
	v_mul_f32_e32 v25, 0x3b000000, v25
	v_add_f32_e32 v26, v26, v30
	v_mul_f32_e32 v34, v58, v34
	v_mul_f32_e32 v26, 0x3b000000, v26
	ds_write_b32 v21, v24
	ds_write_b32 v21, v25 offset:1024
	ds_write_b32 v21, v26 offset:2048
	s_mov_b64 exec, s[20:21]
	ds_write_b32 v57, v34
	s_mov_b64 exec, -1
	s_waitcnt lgkmcnt(0)
	s_barrier
	ds_read2st64_b32 v[60:61], v22 offset0:0 offset1:1
	ds_read2st64_b32 v[62:63], v22 offset0:2 offset1:3
	ds_read2st64_b32 v[64:65], v22 offset0:4 offset1:5
	ds_read2st64_b32 v[66:67], v22 offset0:6 offset1:7
	ds_read2st64_b32 v[68:69], v22 offset0:8 offset1:9
	ds_read2st64_b32 v[70:71], v22 offset0:10 offset1:11
	ds_read2_b32 v[72:73], v23 offset0:0 offset1:16
	ds_read2_b32 v[74:75], v23 offset0:4 offset1:20
	ds_read2_b32 v[76:77], v23 offset0:8 offset1:24
	ds_read2_b32 v[78:79], v23 offset0:12 offset1:28
	s_waitcnt vmcnt(0)
	s_waitcnt lgkmcnt(9)
	v_mfma_f32_16x16x4_f32 v[80:83], v36, v60, 0
	v_mfma_f32_16x16x4_f32 v[84:87], v40, v61, 0
	s_waitcnt lgkmcnt(8)
	v_mfma_f32_16x16x4_f32 v[80:83], v44, v62, v[80:83]
	v_mfma_f32_16x16x4_f32 v[84:87], v48, v63, v[84:87]
	s_waitcnt lgkmcnt(7)
	v_mfma_f32_16x16x4_f32 v[80:83], v38, v64, v[80:83]
	v_mfma_f32_16x16x4_f32 v[84:87], v42, v65, v[84:87]
	v_cndmask_b32_e64 v88, 0, v56, s[22:23]
	s_waitcnt lgkmcnt(6)
	v_mfma_f32_16x16x4_f32 v[80:83], v46, v66, v[80:83]
	v_mfma_f32_16x16x4_f32 v[84:87], v50, v67, v[84:87]
	s_waitcnt lgkmcnt(5)
	v_mfma_f32_16x16x4_f32 v[80:83], v39, v68, v[80:83]
	v_mfma_f32_16x16x4_f32 v[84:87], v43, v69, v[84:87]
	s_waitcnt lgkmcnt(4)
	v_mfma_f32_16x16x4_f32 v[80:83], v47, v70, v[80:83]
	v_mfma_f32_16x16x4_f32 v[84:87], v51, v71, v[84:87]
	s_waitcnt lgkmcnt(0)
	v_fmac_f32_e32 v88, v37, v72
	v_fmac_f32_e32 v88, v52, v73
	v_fmac_f32_e32 v88, v41, v74
	v_fmac_f32_e32 v88, v53, v75
	v_fmac_f32_e32 v88, v45, v76
	v_fmac_f32_e32 v88, v54, v77
	v_fmac_f32_e32 v88, v49, v78
	v_fmac_f32_e32 v88, v55, v79
	s_nop 1
	v_mfma_f32_16x16x4_f32 v[80:83], v88, v89, v[80:83]
	s_nop 7
	s_nop 1
	v_add_f32_e32 v80, v80, v84
	v_add_f32_e32 v81, v81, v85
	v_add_f32_e32 v82, v82, v86
	v_add_f32_e32 v83, v83, v87
	v_max_f32_e32 v80, 0, v80
	v_max_f32_e32 v81, 0, v81
	v_max_f32_e32 v82, 0, v82
	v_max_f32_e32 v83, 0, v83
	global_store_dwordx4 v59, v[80:83], s[10:11] sc1
	v_mul_f32_e32 v84, v80, v80
	v_mul_f32_e32 v85, v81, v81
	v_mul_f32_e32 v86, v82, v82
	v_mul_f32_e32 v87, v83, v83
	v_add_f32_dpp v80, v80, v80 quad_perm:[1,0,3,2] row_mask:0xf bank_mask:0xf
	v_add_f32_dpp v81, v81, v81 quad_perm:[1,0,3,2] row_mask:0xf bank_mask:0xf
	v_add_f32_dpp v82, v82, v82 quad_perm:[1,0,3,2] row_mask:0xf bank_mask:0xf
	v_add_f32_dpp v83, v83, v83 quad_perm:[1,0,3,2] row_mask:0xf bank_mask:0xf
	v_add_f32_dpp v84, v84, v84 quad_perm:[1,0,3,2] row_mask:0xf bank_mask:0xf
	v_add_f32_dpp v85, v85, v85 quad_perm:[1,0,3,2] row_mask:0xf bank_mask:0xf
	v_add_f32_dpp v86, v86, v86 quad_perm:[1,0,3,2] row_mask:0xf bank_mask:0xf
	v_add_f32_dpp v87, v87, v87 quad_perm:[1,0,3,2] row_mask:0xf bank_mask:0xf
	v_add_f32_dpp v80, v80, v80 quad_perm:[2,3,0,1] row_mask:0xf bank_mask:0xf
	v_add_f32_dpp v81, v81, v81 quad_perm:[2,3,0,1] row_mask:0xf bank_mask:0xf
	v_add_f32_dpp v82, v82, v82 quad_perm:[2,3,0,1] row_mask:0xf bank_mask:0xf
	v_add_f32_dpp v83, v83, v83 quad_perm:[2,3,0,1] row_mask:0xf bank_mask:0xf
	v_add_f32_dpp v84, v84, v84 quad_perm:[2,3,0,1] row_mask:0xf bank_mask:0xf
	v_add_f32_dpp v85, v85, v85 quad_perm:[2,3,0,1] row_mask:0xf bank_mask:0xf
	v_add_f32_dpp v86, v86, v86 quad_perm:[2,3,0,1] row_mask:0xf bank_mask:0xf
	v_add_f32_dpp v87, v87, v87 quad_perm:[2,3,0,1] row_mask:0xf bank_mask:0xf
	v_add_f32_dpp v80, v80, v80 row_half_mirror row_mask:0xf bank_mask:0xf
	v_add_f32_dpp v81, v81, v81 row_half_mirror row_mask:0xf bank_mask:0xf
	v_add_f32_dpp v82, v82, v82 row_half_mirror row_mask:0xf bank_mask:0xf
	v_add_f32_dpp v83, v83, v83 row_half_mirror row_mask:0xf bank_mask:0xf
	v_add_f32_dpp v84, v84, v84 row_half_mirror row_mask:0xf bank_mask:0xf
	v_add_f32_dpp v85, v85, v85 row_half_mirror row_mask:0xf bank_mask:0xf
	v_add_f32_dpp v86, v86, v86 row_half_mirror row_mask:0xf bank_mask:0xf
	v_add_f32_dpp v87, v87, v87 row_half_mirror row_mask:0xf bank_mask:0xf
	v_add_f32_dpp v80, v80, v80 row_mirror row_mask:0xf bank_mask:0xf
	v_add_f32_dpp v81, v81, v81 row_mirror row_mask:0xf bank_mask:0xf
	v_add_f32_dpp v82, v82, v82 row_mirror row_mask:0xf bank_mask:0xf
	v_add_f32_dpp v83, v83, v83 row_mirror row_mask:0xf bank_mask:0xf
	v_add_f32_dpp v84, v84, v84 row_mirror row_mask:0xf bank_mask:0xf
	v_add_f32_dpp v85, v85, v85 row_mirror row_mask:0xf bank_mask:0xf
	v_add_f32_dpp v86, v86, v86 row_mirror row_mask:0xf bank_mask:0xf
	v_add_f32_dpp v87, v87, v87 row_mirror row_mask:0xf bank_mask:0xf
	s_mov_b32 s24, 0x00020002
	s_mov_b32 s25, 0x00020002
	v_cndmask_b32_e64 v80, v80, v81, s[24:25]
	s_mov_b32 s24, 0x00040004
	s_mov_b32 s25, 0x00040004
	v_cndmask_b32_e64 v80, v80, v82, s[24:25]
	s_mov_b32 s24, 0x00080008
	s_mov_b32 s25, 0x00080008
	v_cndmask_b32_e64 v80, v80, v83, s[24:25]
	s_mov_b32 s24, 0x00100010
	s_mov_b32 s25, 0x00100010
	v_cndmask_b32_e64 v80, v80, v84, s[24:25]
	s_mov_b32 s24, 0x00200020
	s_mov_b32 s25, 0x00200020
	v_cndmask_b32_e64 v80, v80, v85, s[24:25]
	s_mov_b32 s24, 0x00400040
	s_mov_b32 s25, 0x00400040
	v_cndmask_b32_e64 v80, v80, v86, s[24:25]
	s_mov_b32 s24, 0x00800080
	s_mov_b32 s25, 0x00800080
	v_cndmask_b32_e64 v80, v80, v87, s[24:25]
	s_mov_b32 s24, 0x000f000f
	s_mov_b32 s25, 0x000f000f
	s_mov_b64 exec, s[24:25]
	global_atomic_add_f32 v90, v80, s[12:13]
	s_mov_b32 s24, 0x00f000f0
	s_mov_b32 s25, 0x00f000f0
	s_mov_b64 exec, s[24:25]
	global_atomic_add_f32 v90, v80, s[14:15]
	s_endpgm

_Z7k_layerPKfS0_S0_S0_S0_S0_S0_PfS1_S1_:
	s_load_dwordx4 s[28:31], s[0:1], 0x40
	s_load_dwordx2 s[10:11], s[0:1], 0x0
	s_load_dwordx4 s[12:15], s[0:1], 0x28
	s_load_dwordx2 s[8:9], s[0:1], 0x38
	v_cmp_lt_u32_e64 s[6:7], 63, v0
	v_cmp_gt_u32_e64 s[4:5], 64, v0
	v_mov_b32_e32 v70, 0x7fc00000
	v_lshlrev_b32_e32 v18, 2, v0
	s_and_saveexec_b64 s[16:17], s[4:5]
	s_cbranch_execz .LBB2_2
	s_load_dwordx8 s[20:27], s[0:1], 0x8
	s_waitcnt lgkmcnt(0)
	v_add_u32_e32 v77, 0x3000, v18
	global_load_dword v81, v77, s[20:21] offset:256 sc1
	global_load_dword v80, v77, s[22:23] offset:256 sc1
	global_load_dword v83, v77, s[20:21] offset:512 sc1
	global_load_dword v82, v77, s[22:23] offset:512 sc1
	global_load_dword v85, v77, s[20:21] offset:768 sc1
	global_load_dword v84, v77, s[22:23] offset:768 sc1
	global_load_dword v87, v77, s[20:21] offset:1024 sc1
	global_load_dword v86, v77, s[22:23] offset:1024 sc1
	global_load_dword v89, v77, s[20:21] offset:1280 sc1
	global_load_dword v88, v77, s[22:23] offset:1280 sc1
	global_load_dword v91, v77, s[20:21] offset:1536 sc1
	global_load_dword v90, v77, s[22:23] offset:1536 sc1
	global_load_dword v93, v77, s[20:21] offset:1792 sc1
	global_load_dword v92, v77, s[22:23] offset:1792 sc1
	global_load_dword v95, v77, s[20:21] sc1
	global_load_dword v94, v77, s[22:23] sc1
	global_load_dword v48, v18, s[20:21] sc1
	global_load_dword v1, v18, s[22:23] sc1
	global_load_dword v73, v18, s[20:21] offset:256 sc1
	global_load_dword v72, v18, s[22:23] offset:256 sc1
	global_load_dword v69, v18, s[20:21] offset:512 sc1
	global_load_dword v68, v18, s[22:23] offset:512 sc1
	global_load_dword v67, v18, s[20:21] offset:768 sc1
	global_load_dword v66, v18, s[22:23] offset:768 sc1
	global_load_dword v65, v18, s[20:21] offset:1024 sc1
	global_load_dword v64, v18, s[22:23] offset:1024 sc1
	global_load_dword v63, v18, s[20:21] offset:1280 sc1
	global_load_dword v62, v18, s[22:23] offset:1280 sc1
	global_load_dword v61, v18, s[20:21] offset:1536 sc1
	global_load_dword v60, v18, s[22:23] offset:1536 sc1
	global_load_dword v53, v18, s[20:21] offset:1792 sc1
	global_load_dword v52, v18, s[22:23] offset:1792 sc1
	global_load_dword v49, v18, s[24:25]
	global_load_dword v76, v18, s[26:27]
	s_waitcnt vmcnt(16)
	v_add_f32_e32 v70, 0, v1
.LBB2_2:
	s_or_b64 exec, exec, s[16:17]
	s_lshl_b32 s16, s2, 4
	v_and_b32_e32 v19, 15, v0
	v_or_b32_e32 v22, s16, v19
	v_lshrrev_b32_e32 v1, 2, v0
	v_ashrrev_i32_e32 v23, 31, v22
	v_bfe_u32 v75, v0, 4, 2
	v_and_b32_e32 v74, 48, v1
	v_lshlrev_b64 v[2:3], 8, v[22:23]
	v_or_b32_e32 v71, v74, v19
	s_waitcnt lgkmcnt(0)
	v_lshl_add_u64 v[2:3], s[10:11], 0, v[2:3]
	v_lshlrev_b32_e32 v20, 6, v75
	v_mov_b32_e32 v21, 0
	v_lshl_add_u64 v[24:25], v[2:3], 0, v[20:21]
	v_lshlrev_b32_e32 v20, 3, v71
	v_lshl_or_b32 v20, v75, 13, v20
	global_load_dwordx4 v[2:5], v[24:25], off offset:48
	global_load_dwordx4 v[6:9], v[24:25], off offset:32
	global_load_dwordx4 v[10:13], v[24:25], off offset:16
	global_load_dwordx4 v[14:17], v[24:25], off
	v_lshl_add_u64 v[24:25], s[12:13], 0, v[20:21]
	s_movk_i32 s3, 0x1000
	v_add_co_u32_e32 v78, vcc, s3, v24
	global_load_dwordx2 v[58:59], v20, s[12:13]
	global_load_dwordx2 v[56:57], v20, s[12:13] offset:512
	global_load_dwordx2 v[54:55], v20, s[12:13] offset:1024
	global_load_dwordx2 v[50:51], v20, s[12:13] offset:1536
	global_load_dwordx2 v[46:47], v20, s[12:13] offset:2048
	global_load_dwordx2 v[44:45], v20, s[12:13] offset:2560
	global_load_dwordx2 v[42:43], v20, s[12:13] offset:3072
	global_load_dwordx2 v[36:37], v20, s[12:13] offset:3584
	v_addc_co_u32_e32 v79, vcc, 0, v25, vcc
	global_load_dwordx2 v[40:41], v[78:79], off
	global_load_dwordx2 v[38:39], v[78:79], off offset:512
	global_load_dwordx2 v[34:35], v[78:79], off offset:1024
	global_load_dwordx2 v[32:33], v[78:79], off offset:1536
	global_load_dwordx2 v[30:31], v[78:79], off offset:2048
	global_load_dwordx2 v[28:29], v[78:79], off offset:2560
	global_load_dwordx2 v[24:25], v[78:79], off offset:3072
	global_load_dwordx2 v[26:27], v[78:79], off offset:3584
	v_lshlrev_b32_e32 v20, 2, v71
	global_load_dword v20, v20, s[14:15]
	s_bfe_i32 s12, s2, 0x170005
	v_lshlrev_b32_e32 v23, 4, v75
	s_and_saveexec_b64 s[2:3], s[4:5]
	s_cbranch_execz .LBB2_4
	s_waitcnt vmcnt(23)
	v_add_f32_e32 v70, v70, v94
	v_add_f32_e32 v48, v48, v95
	v_pk_add_f32 v[72:73], v[72:73], v[80:81]
	v_pk_add_f32 v[68:69], v[68:69], v[82:83]
	v_pk_add_f32 v[66:67], v[66:67], v[84:85]
	v_pk_add_f32 v[64:65], v[64:65], v[86:87]
	v_pk_add_f32 v[62:63], v[62:63], v[88:89]
	v_pk_add_f32 v[60:61], v[60:61], v[90:91]
	v_pk_add_f32 v[52:53], v[52:53], v[92:93]
	s_cmpk_lt_u32 s16, 0x200
	s_cselect_b64 vcc, -1, 0
	s_cmp_eq_u32 s12, 1
	v_add_f32_e32 v71, 0, v48
	v_cndmask_b32_e32 v48, 0, v48, vcc
	s_cselect_b64 vcc, -1, 0
	s_cmp_eq_u32 s12, 2
	s_waitcnt vmcnt(36)
	v_cndmask_b32_e32 v48, v48, v73, vcc
	s_cselect_b64 vcc, -1, 0
	s_cmp_eq_u32 s12, 3
	s_waitcnt vmcnt(35)
	v_pk_add_f32 v[70:71], v[72:73], v[70:71]
	s_waitcnt vmcnt(34)
	v_cndmask_b32_e32 v48, v48, v69, vcc
	s_cselect_b64 vcc, -1, 0
	s_cmp_eq_u32 s12, 4
	s_waitcnt vmcnt(33)
	v_pk_add_f32 v[68:69], v[68:69], v[70:71]
	s_waitcnt vmcnt(32)
	v_cndmask_b32_e32 v48, v48, v67, vcc
	s_cselect_b64 vcc, -1, 0
	s_cmp_eq_u32 s12, 5
	s_waitcnt vmcnt(31)
	v_pk_add_f32 v[66:67], v[66:67], v[68:69]
	s_waitcnt vmcnt(30)
	v_cndmask_b32_e32 v48, v48, v65, vcc
	s_cselect_b64 vcc, -1, 0
	s_cmp_eq_u32 s12, 6
	s_waitcnt vmcnt(29)
	v_pk_add_f32 v[64:65], v[64:65], v[66:67]
	s_waitcnt vmcnt(28)
	v_cndmask_b32_e32 v48, v48, v63, vcc
	s_cselect_b64 vcc, -1, 0
	s_waitcnt vmcnt(27)
	v_pk_add_f32 v[62:63], v[62:63], v[64:65]
	s_waitcnt vmcnt(26)
	v_cndmask_b32_e32 v48, v48, v61, vcc
	s_waitcnt vmcnt(25)
	v_pk_add_f32 v[60:61], v[60:61], v[62:63]
	s_mov_b32 s4, 0x39800000
	s_waitcnt vmcnt(23)
	v_pk_add_f32 v[60:61], v[52:53], v[60:61]
	s_cmp_eq_u32 s12, 7
	v_pk_mul_f32 v[60:61], v[60:61], s[4:5] op_sel_hi:[1,0]
	s_cselect_b64 vcc, -1, 0
	v_fma_f32 v52, -v61, v61, v60
	v_max_f32_e32 v52, 0, v52
	v_add_f32_e32 v52, 0x3727c5ac, v52
	v_rsq_f32_e32 v63, v52
	v_cndmask_b32_e32 v48, v48, v53, vcc
	v_mov_b32_e32 v62, 0x3b000000
	s_waitcnt vmcnt(22)
	v_pk_mul_f32 v[48:49], v[48:49], v[62:63]
	s_waitcnt vmcnt(21)
	v_fma_f32 v52, -v61, v49, v76
	ds_write2st64_b32 v18, v49, v52 offset0:2 offset1:3
	v_fmac_f32_e32 v52, v48, v49
	ds_write_b32 v18, v52 offset:1024
.LBB2_4:
	s_or_b64 exec, exec, s[2:3]
	v_lshlrev_b32_e32 v23, 2, v23
	s_waitcnt lgkmcnt(0)
	s_barrier
	s_waitcnt vmcnt(25)
	ds_read_b128 v[60:63], v23 offset:512
	ds_read_b128 v[64:67], v23 offset:528
	v_cmp_eq_u32_e32 vcc, 0, v75
	s_and_b32 s9, s9, 0xffff
	s_mov_b32 s11, 0x20000
	s_waitcnt vmcnt(16) lgkmcnt(1)
	v_mul_f32_e32 v48, v58, v60
	s_waitcnt vmcnt(0)
	v_cndmask_b32_e32 v20, 0, v20, vcc
	s_mov_b32 s10, 0x100000
	v_mfma_f32_16x16x4_f32 a[0:3], v48, v14, 0
	v_mul_f32_e32 v14, v56, v61
	v_cmp_eq_u32_e32 vcc, 0, v19
	s_nop 0
	v_mfma_f32_16x16x4_f32 a[4:7], v14, v15, 0
	v_mul_f32_e32 v14, v54, v62
	s_nop 1
	v_mfma_f32_16x16x4_f32 a[0:3], v14, v16, a[0:3]
	v_mul_f32_e32 v14, v50, v63
	s_nop 1
	v_mfma_f32_16x16x4_f32 a[4:7], v14, v17, a[4:7]
	s_waitcnt lgkmcnt(0)
	v_mul_f32_e32 v14, v46, v64
	s_nop 1
	v_mfma_f32_16x16x4_f32 a[0:3], v14, v10, a[0:3]
	v_mul_f32_e32 v10, v44, v65
	ds_read_b128 v[14:17], v23 offset:1024
	ds_read_b128 v[60:63], v23 offset:768
	ds_read_b128 v[68:71], v23 offset:1040
	ds_read_b128 v[76:79], v23 offset:784
	v_mfma_f32_16x16x4_f32 a[4:7], v10, v11, a[4:7]
	v_mul_f32_e32 v11, v42, v66
	s_waitcnt lgkmcnt(3)
	v_mul_f32_e32 v10, v59, v14
	s_waitcnt lgkmcnt(2)
	v_fmac_f32_e32 v10, v58, v60
	v_mul_f32_e32 v14, v57, v15
	v_add_f32_e32 v10, v20, v10
	v_fmac_f32_e32 v14, v56, v61
	v_add_f32_e32 v10, v14, v10
	v_mfma_f32_16x16x4_f32 a[0:3], v11, v12, a[0:3]
	v_mul_f32_e32 v11, v55, v16
	v_mul_f32_e32 v12, v36, v67
	v_fmac_f32_e32 v11, v54, v62
	ds_read_b128 v[52:55], v23 offset:544
	v_add_f32_e32 v14, v11, v10
	v_mul_f32_e32 v15, v51, v17
	v_fmac_f32_e32 v15, v50, v63
	v_mfma_f32_16x16x4_f32 a[4:7], v12, v13, a[4:7]
	ds_read_b128 v[10:13], v23 offset:560
	s_waitcnt lgkmcnt(1)
	v_mul_f32_e32 v16, v40, v52
	v_add_f32_e32 v14, v15, v14
	v_mul_f32_e32 v15, v47, v68
	v_fmac_f32_e32 v15, v46, v76
	v_add_f32_e32 v14, v14, v15
	v_mul_f32_e32 v15, v38, v53
	v_mfma_f32_16x16x4_f32 a[0:3], v16, v6, a[0:3]
	v_mul_f32_e32 v20, v34, v54
	v_mul_f32_e32 v6, v45, v69
	v_fmac_f32_e32 v6, v44, v77
	v_add_f32_e32 v6, v6, v14
	v_mul_f32_e32 v14, v43, v70
	v_fmac_f32_e32 v14, v42, v78
	v_add_f32_e32 v6, v14, v6
	v_mfma_f32_16x16x4_f32 a[4:7], v15, v7, a[4:7]
	ds_read_b128 v[14:17], v23 offset:800
	ds_read_b128 v[42:45], v23 offset:1056
	v_mul_f32_e32 v7, v37, v71
	v_fmac_f32_e32 v7, v36, v79
	v_add_f32_e32 v48, v7, v6
	v_mov_b32_e32 v6, v40
	v_mov_b32_e32 v40, v41
	v_mov_b32_e32 v41, v39
	v_mfma_f32_16x16x4_f32 a[0:3], v20, v8, a[0:3]
	v_mul_f32_e32 v8, v32, v55
	v_mov_b32_e32 v7, v38
	s_waitcnt lgkmcnt(0)
	v_mul_f32_e64 v46, v40, v42
	v_mul_f32_e64 v47, v41, v43
	v_mul_f32_e32 v11, v28, v11
	v_pk_fma_f32 v[6:7], v[6:7], v[14:15], v[46:47]
	ds_read_b128 v[36:39], v23 offset:1072
	ds_read_b128 v[40:43], v23 offset:816
	v_mfma_f32_16x16x4_f32 a[4:7], v8, v9, a[4:7]
	v_mul_f32_e32 v8, v30, v10
	v_add_f32_e32 v6, v48, v6
	v_add_f32_e32 v10, v7, v6
	v_mov_b32_e32 v7, v32
	v_mov_b32_e32 v32, v35
	v_mov_b32_e32 v6, v34
	v_mov_b32_e32 v23, v21
	v_mfma_f32_16x16x4_f32 a[0:3], v8, v2, a[0:3]
	v_mul_f32_e64 v8, v32, v44
	v_mul_f32_e64 v9, v33, v45
	v_mov_b32_e32 v20, 0
	v_fma_f32 v6, v6, v16, v8
	v_fma_f32 v7, v7, v17, v9
	v_mul_f32_e32 v9, v24, v12
	v_add_f32_e32 v2, v6, v10
	v_add_f32_e32 v8, v7, v2
	v_mov_b32_e32 v2, v30
	v_mfma_f32_16x16x4_f32 a[4:7], v11, v3, a[4:7]
	v_mov_b32_e32 v3, v28
	v_mov_b32_e32 v28, v31
	s_waitcnt lgkmcnt(1)
	v_mul_f32_e64 v6, v28, v36
	v_mul_f32_e64 v7, v29, v37
	v_mov_b32_e32 v16, v21
	s_waitcnt lgkmcnt(0)
	v_pk_fma_f32 v[2:3], v[2:3], v[40:41], v[6:7]
	v_mov_b32_e32 v17, v21
	v_add_f32_e32 v2, v8, v2
	v_mfma_f32_16x16x4_f32 a[0:3], v9, v4, a[0:3]
	v_add_f32_e32 v4, v3, v2
	v_mul_f32_e32 v8, v26, v13
	v_mov_b32_e32 v3, v26
	v_mov_b32_e32 v26, v25
	v_mov_b32_e32 v2, v24
	v_pk_mul_f32 v[6:7], v[26:27], v[38:39]
	v_mov_b32_e32 v9, v21
	v_pk_fma_f32 v[2:3], v[2:3], v[42:43], v[6:7]
	v_mfma_f32_16x16x4_f32 a[4:7], v8, v5, a[4:7]
	v_add_f32_e32 v2, v2, v4
	v_add_f32_e32 v4, v3, v2
	v_mov_b32_e32 v5, 1.0
	v_mov_b32_e32 v8, v21
	s_nop 0
	v_mfma_f32_16x16x4_f32 a[0:3], v4, v5, a[0:3]
	s_nop 3
	v_accvgpr_read_b32 v3, a7
	v_accvgpr_read_b32 v2, a6
	v_accvgpr_read_b32 v7, a5
	v_accvgpr_read_b32 v6, a4
	s_nop 1
	v_accvgpr_read_b32 v5, a3
	v_accvgpr_read_b32 v4, a2
	v_pk_add_f32 v[2:3], v[2:3], v[4:5]
	v_accvgpr_read_b32 v5, a1
	v_accvgpr_read_b32 v4, a0
	v_pk_add_f32 v[4:5], v[6:7], v[4:5]
	v_max_f32_e32 v14, 0, v2
	v_max_f32_e32 v12, 0, v4
	v_max_f32_e32 v13, 0, v5
	v_max_f32_e32 v15, 0, v3
	v_lshlrev_b32_e32 v2, 6, v22
	v_and_b32_e32 v3, 12, v1
	v_or3_b32 v2, v2, v74, v3
	v_lshlrev_b32_e32 v2, 2, v2
	buffer_store_dwordx4 v[12:15], v2, s[8:11], 0 offen sc1
	v_mul_f32_e32 v4, v12, v12
	v_mul_f32_e32 v5, v13, v13
	v_mul_f32_e32 v6, v14, v14
	v_mul_f32_e32 v7, v15, v15
	v_and_b32_e32 v8, 3, v19
	v_and_b32_e32 v9, 12, v1
	v_or3_b32 v8, v8, v9, v74
	s_lshl_b32 s2, s12, 8
	s_bfe_u32 s3, s16, 0x10004
	s_mul_i32 s3, s3, 0x3000
	s_add_u32 s2, s2, s3
	v_lshl_add_u32 v8, v8, 2, s2
	v_add_f32_dpp v12, v12, v12 quad_perm:[1,0,3,2] row_mask:0xf bank_mask:0xf
	v_add_f32_dpp v13, v13, v13 quad_perm:[1,0,3,2] row_mask:0xf bank_mask:0xf
	v_add_f32_dpp v14, v14, v14 quad_perm:[1,0,3,2] row_mask:0xf bank_mask:0xf
	v_add_f32_dpp v15, v15, v15 quad_perm:[1,0,3,2] row_mask:0xf bank_mask:0xf
	v_add_f32_dpp v4, v4, v4 quad_perm:[1,0,3,2] row_mask:0xf bank_mask:0xf
	v_add_f32_dpp v5, v5, v5 quad_perm:[1,0,3,2] row_mask:0xf bank_mask:0xf
	v_add_f32_dpp v6, v6, v6 quad_perm:[1,0,3,2] row_mask:0xf bank_mask:0xf
	v_add_f32_dpp v7, v7, v7 quad_perm:[1,0,3,2] row_mask:0xf bank_mask:0xf
	v_add_f32_dpp v12, v12, v12 quad_perm:[2,3,0,1] row_mask:0xf bank_mask:0xf
	v_add_f32_dpp v13, v13, v13 quad_perm:[2,3,0,1] row_mask:0xf bank_mask:0xf
	v_add_f32_dpp v14, v14, v14 quad_perm:[2,3,0,1] row_mask:0xf bank_mask:0xf
	v_add_f32_dpp v15, v15, v15 quad_perm:[2,3,0,1] row_mask:0xf bank_mask:0xf
	v_add_f32_dpp v4, v4, v4 quad_perm:[2,3,0,1] row_mask:0xf bank_mask:0xf
	v_add_f32_dpp v5, v5, v5 quad_perm:[2,3,0,1] row_mask:0xf bank_mask:0xf
	v_add_f32_dpp v6, v6, v6 quad_perm:[2,3,0,1] row_mask:0xf bank_mask:0xf
	v_add_f32_dpp v7, v7, v7 quad_perm:[2,3,0,1] row_mask:0xf bank_mask:0xf
	v_add_f32_dpp v12, v12, v12 row_half_mirror row_mask:0xf bank_mask:0xf
	v_add_f32_dpp v13, v13, v13 row_half_mirror row_mask:0xf bank_mask:0xf
	v_add_f32_dpp v14, v14, v14 row_half_mirror row_mask:0xf bank_mask:0xf
	v_add_f32_dpp v15, v15, v15 row_half_mirror row_mask:0xf bank_mask:0xf
	v_add_f32_dpp v4, v4, v4 row_half_mirror row_mask:0xf bank_mask:0xf
	v_add_f32_dpp v5, v5, v5 row_half_mirror row_mask:0xf bank_mask:0xf
	v_add_f32_dpp v6, v6, v6 row_half_mirror row_mask:0xf bank_mask:0xf
	v_add_f32_dpp v7, v7, v7 row_half_mirror row_mask:0xf bank_mask:0xf
	v_add_f32_dpp v12, v12, v12 row_mirror row_mask:0xf bank_mask:0xf
	v_add_f32_dpp v13, v13, v13 row_mirror row_mask:0xf bank_mask:0xf
	v_add_f32_dpp v14, v14, v14 row_mirror row_mask:0xf bank_mask:0xf
	v_add_f32_dpp v15, v15, v15 row_mirror row_mask:0xf bank_mask:0xf
	v_add_f32_dpp v4, v4, v4 row_mirror row_mask:0xf bank_mask:0xf
	v_add_f32_dpp v5, v5, v5 row_mirror row_mask:0xf bank_mask:0xf
	v_add_f32_dpp v6, v6, v6 row_mirror row_mask:0xf bank_mask:0xf
	v_add_f32_dpp v7, v7, v7 row_mirror row_mask:0xf bank_mask:0xf
	s_mov_b32 s32, 0x00020002
	s_mov_b32 s33, 0x00020002
	v_cndmask_b32_e64 v12, v12, v13, s[32:33]
	s_mov_b32 s32, 0x00040004
	s_mov_b32 s33, 0x00040004
	v_cndmask_b32_e64 v12, v12, v14, s[32:33]
	s_mov_b32 s32, 0x00080008
	s_mov_b32 s33, 0x00080008
	v_cndmask_b32_e64 v12, v12, v15, s[32:33]
	s_mov_b32 s32, 0x00100010
	s_mov_b32 s33, 0x00100010
	v_cndmask_b32_e64 v12, v12, v4, s[32:33]
	s_mov_b32 s32, 0x00200020
	s_mov_b32 s33, 0x00200020
	v_cndmask_b32_e64 v12, v12, v5, s[32:33]
	s_mov_b32 s32, 0x00400040
	s_mov_b32 s33, 0x00400040
	v_cndmask_b32_e64 v12, v12, v6, s[32:33]
	s_mov_b32 s32, 0x00800080
	s_mov_b32 s33, 0x00800080
	v_cndmask_b32_e64 v12, v12, v7, s[32:33]
	s_mov_b32 s2, 0x000f000f
	s_mov_b32 s3, 0x000f000f
	s_mov_b64 exec, s[2:3]
	global_atomic_add_f32 v8, v12, s[28:29]
	s_mov_b32 s2, 0x00f000f0
	s_mov_b32 s3, 0x00f000f0
	s_mov_b64 exec, s[2:3]
	global_atomic_add_f32 v8, v12, s[30:31]
	s_endpgm

	.amdhsa_kernel _Z7k_layerPKfS0_S0_S0_S0_S0_S0_PfS1_S1_
		.amdhsa_group_segment_fixed_size 1280
		.amdhsa_private_segment_fixed_size 0
		.amdhsa_kernarg_size 80
		.amdhsa_user_sgpr_count 2
		.amdhsa_user_sgpr_dispatch_ptr 0
		.amdhsa_user_sgpr_queue_ptr 0
		.amdhsa_user_sgpr_kernarg_segment_ptr 1
		.amdhsa_user_sgpr_dispatch_id 0
		.amdhsa_user_sgpr_kernarg_preload_length 0
		.amdhsa_user_sgpr_kernarg_preload_offset 0
		.amdhsa_user_sgpr_private_segment_size 0
		.amdhsa_uses_dynamic_stack 0
		.amdhsa_enable_private_segment 0
		.amdhsa_system_sgpr_workgroup_id_x 1
		.amdhsa_system_sgpr_workgroup_id_y 0
		.amdhsa_system_sgpr_workgroup_id_z 0
		.amdhsa_system_sgpr_workgroup_info 0
		.amdhsa_system_vgpr_workitem_id 0
		.amdhsa_next_free_vgpr 104
		.amdhsa_next_free_sgpr 34
		.amdhsa_accum_offset 96
		.amdhsa_reserve_vcc 1
		.amdhsa_float_round_mode_32 0
		.amdhsa_float_round_mode_16_64 0
		.amdhsa_float_denorm_mode_32 3
		.amdhsa_float_denorm_mode_16_64 3
		.amdhsa_dx10_clamp 1
		.amdhsa_ieee_mode 1
		.amdhsa_fp16_overflow 0
		.amdhsa_tg_split 0
		.amdhsa_exception_fp_ieee_invalid_op 0
		.amdhsa_exception_fp_denorm_src 0
		.amdhsa_exception_fp_ieee_div_zero 0
		.amdhsa_exception_fp_ieee_overflow 0
		.amdhsa_exception_fp_ieee_underflow 0
		.amdhsa_exception_fp_ieee_inexact 0
		.amdhsa_exception_int_div_zero 0
	.end_amdhsa_kernel

_Z8k5_finalPKfS0_S0_S0_S0_S0_S0_S0_S0_Pf:
	s_load_dwordx8 s[4:11], s[0:1], 0x28
	s_load_dwordx2 s[12:13], s[0:1], 0x0
	s_load_dwordx8 s[16:23], s[0:1], 0x8
	v_lshrrev_b32_e32 v63, 4, v0
	v_lshlrev_b32_e32 v63, 2, v63
	v_cmp_gt_u32_e32 vcc, 64, v0
	v_mov_b32_e32 v54, 0x7fc00000
	v_lshlrev_b32_e32 v58, 2, v0
	v_mov_b32_e32 v55, 0x7fc00000
	s_waitcnt lgkmcnt(0)
	global_load_dword v63, v63, s[10:11]
	s_and_saveexec_b64 s[14:15], vcc
	s_cbranch_execz .LBB3_2
	v_add_u32_e32 v64, 0x3000, v58
	global_load_dword v67, v64, s[16:17] sc1
	global_load_dword v66, v64, s[18:19] sc1
	global_load_dword v69, v64, s[16:17] offset:256 sc1
	global_load_dword v68, v64, s[18:19] offset:256 sc1
	global_load_dword v71, v64, s[16:17] offset:512 sc1
	global_load_dword v70, v64, s[18:19] offset:512 sc1
	global_load_dword v73, v64, s[16:17] offset:768 sc1
	global_load_dword v72, v64, s[18:19] offset:768 sc1
	global_load_dword v75, v64, s[16:17] offset:1024 sc1
	global_load_dword v74, v64, s[18:19] offset:1024 sc1
	global_load_dword v77, v64, s[16:17] offset:1280 sc1
	global_load_dword v76, v64, s[18:19] offset:1280 sc1
	global_load_dword v79, v64, s[16:17] offset:1536 sc1
	global_load_dword v78, v64, s[18:19] offset:1536 sc1
	global_load_dword v81, v64, s[16:17] offset:1792 sc1
	global_load_dword v80, v64, s[18:19] offset:1792 sc1
	global_load_dword v3, v58, s[16:17] sc1
	global_load_dword v2, v58, s[18:19] sc1
	global_load_dword v53, v58, s[16:17] offset:256 sc1
	global_load_dword v52, v58, s[18:19] offset:256 sc1
	global_load_dword v51, v58, s[16:17] offset:512 sc1
	global_load_dword v50, v58, s[18:19] offset:512 sc1
	global_load_dword v49, v58, s[16:17] offset:768 sc1
	global_load_dword v48, v58, s[18:19] offset:768 sc1
	global_load_dword v47, v58, s[16:17] offset:1024 sc1
	global_load_dword v46, v58, s[18:19] offset:1024 sc1
	global_load_dword v45, v58, s[16:17] offset:1280 sc1
	global_load_dword v44, v58, s[18:19] offset:1280 sc1
	global_load_dword v43, v58, s[16:17] offset:1536 sc1
	global_load_dword v42, v58, s[18:19] offset:1536 sc1
	global_load_dword v41, v58, s[16:17] offset:1792 sc1
	global_load_dword v40, v58, s[18:19] offset:1792 sc1
	global_load_dword v61, v58, s[20:21]
	global_load_dword v60, v58, s[22:23]
	s_waitcnt vmcnt(16)
	v_pk_add_f32 v[54:55], v[2:3], 0 op_sel_hi:[1,0]
.LBB3_2:
	s_or_b64 exec, exec, s[14:15]
	v_lshrrev_b32_e32 v1, 6, v0
	v_and_b32_e32 v56, 15, v0
	v_lshl_or_b32 v57, v1, 4, v56
	v_bfe_u32 v59, v0, 4, 2
	v_lshlrev_b32_e32 v38, 8, v57
	v_mov_b32_e32 v39, 0
	s_waitcnt lgkmcnt(0)
	v_lshl_add_u64 v[2:3], s[4:5], 0, v[38:39]
	v_lshlrev_b32_e32 v4, 6, v59
	v_mov_b32_e32 v5, v39
	s_lshl_b32 s14, s2, 4
	v_lshl_add_u64 v[2:3], v[2:3], 0, v[4:5]
	global_load_dwordx4 v[6:9], v[2:3], off offset:48
	global_load_dwordx4 v[10:13], v[2:3], off offset:32
	global_load_dwordx4 v[18:21], v[2:3], off offset:16
	global_load_dwordx4 v[22:25], v[2:3], off
	v_or_b32_e32 v2, s14, v56
	v_ashrrev_i32_e32 v3, 31, v2
	v_lshlrev_b64 v[2:3], 8, v[2:3]
	v_lshl_add_u64 v[2:3], s[12:13], 0, v[2:3]
	v_lshl_add_u64 v[2:3], v[2:3], 0, v[4:5]
	global_load_dwordx4 v[14:17], v[2:3], off offset:48
	global_load_dwordx4 v[26:29], v[2:3], off offset:32
	global_load_dwordx4 v[30:33], v[2:3], off offset:16
	global_load_dwordx4 v[34:37], v[2:3], off
	v_lshlrev_b32_e32 v2, 8, v56
	v_mov_b32_e32 v3, v39
	v_lshl_add_u64 v[2:3], s[8:9], 0, v[2:3]
	v_and_b32_e32 v4, 0xc0, v0
	v_lshlrev_b32_e32 v38, 4, v59
	v_lshl_add_u64 v[2:3], v[2:3], 0, v[4:5]
	v_lshl_add_u64 v[2:3], v[2:3], 0, v[38:39]
	v_lshlrev_b32_e32 v57, 2, v57
	global_load_dwordx4 v[2:5], v[2:3], off
	s_load_dwordx2 s[0:1], s[0:1], 0x48
	global_load_dword v62, v57, s[6:7]
	v_lshrrev_b32_e32 v0, 4, v0
	v_lshlrev_b32_e32 v57, 2, v59
	s_and_saveexec_b64 s[2:3], vcc
	s_cbranch_execz .LBB3_4
	s_waitcnt vmcnt(12)
	v_pk_add_f32 v[54:55], v[54:55], v[66:67]
	v_pk_add_f32 v[52:53], v[52:53], v[68:69]
	v_pk_add_f32 v[50:51], v[50:51], v[70:71]
	v_pk_add_f32 v[48:49], v[48:49], v[72:73]
	v_pk_add_f32 v[46:47], v[46:47], v[74:75]
	v_pk_add_f32 v[44:45], v[44:45], v[76:77]
	v_pk_add_f32 v[42:43], v[42:43], v[78:79]
	v_pk_add_f32 v[40:41], v[40:41], v[80:81]
	v_pk_add_f32 v[52:53], v[52:53], v[54:55]
	s_mov_b32 s4, 0x39800000
	s_waitcnt vmcnt(22)
	v_pk_add_f32 v[50:51], v[50:51], v[52:53]
	s_waitcnt vmcnt(20)
	v_pk_add_f32 v[48:49], v[48:49], v[50:51]
	s_waitcnt vmcnt(18)
	v_pk_add_f32 v[46:47], v[46:47], v[48:49]
	s_waitcnt vmcnt(16)
	v_pk_add_f32 v[44:45], v[44:45], v[46:47]
	s_waitcnt vmcnt(14)
	v_pk_add_f32 v[42:43], v[42:43], v[44:45]
	s_waitcnt vmcnt(12)
	v_pk_add_f32 v[40:41], v[40:41], v[42:43]
	s_nop 0
	v_pk_mul_f32 v[40:41], v[40:41], s[4:5] op_sel_hi:[1,0]
	s_nop 0
	v_fma_f32 v40, -v41, v41, v40
	v_max_f32_e32 v40, 0, v40
	v_add_f32_e32 v40, 0x3727c5ac, v40
	v_rsq_f32_e32 v40, v40
	s_waitcnt vmcnt(11)
	v_mul_f32_e32 v40, v61, v40
	s_waitcnt vmcnt(10)
	v_fma_f32 v41, -v41, v40, v60
	ds_write2st64_b32 v58, v40, v41 offset0:16 offset1:17

	.amdhsa_kernel _Z8k5_finalPKfS0_S0_S0_S0_S0_S0_S0_S0_Pf
		.amdhsa_group_segment_fixed_size 4608
		.amdhsa_private_segment_fixed_size 0
		.amdhsa_kernarg_size 80
		.amdhsa_user_sgpr_count 2
		.amdhsa_user_sgpr_dispatch_ptr 0
		.amdhsa_user_sgpr_queue_ptr 0
		.amdhsa_user_sgpr_kernarg_segment_ptr 1
		.amdhsa_user_sgpr_dispatch_id 0
		.amdhsa_user_sgpr_kernarg_preload_length 0
		.amdhsa_user_sgpr_kernarg_preload_offset 0
		.amdhsa_user_sgpr_private_segment_size 0
		.amdhsa_uses_dynamic_stack 0
		.amdhsa_enable_private_segment 0
		.amdhsa_system_sgpr_workgroup_id_x 1
		.amdhsa_system_sgpr_workgroup_id_y 0
		.amdhsa_system_sgpr_workgroup_id_z 0
		.amdhsa_system_sgpr_workgroup_info 0
		.amdhsa_system_vgpr_workitem_id 0
		.amdhsa_next_free_vgpr 96
		.amdhsa_next_free_sgpr 24
		.amdhsa_accum_offset 84
		.amdhsa_reserve_vcc 1
		.amdhsa_float_round_mode_32 0
		.amdhsa_float_round_mode_16_64 0
		.amdhsa_float_denorm_mode_32 3
		.amdhsa_float_denorm_mode_16_64 3
		.amdhsa_dx10_clamp 1
		.amdhsa_ieee_mode 1
		.amdhsa_fp16_overflow 0
		.amdhsa_tg_split 0
		.amdhsa_exception_fp_ieee_invalid_op 0
		.amdhsa_exception_fp_denorm_src 0
		.amdhsa_exception_fp_ieee_div_zero 0
		.amdhsa_exception_fp_ieee_overflow 0
		.amdhsa_exception_fp_ieee_underflow 0
		.amdhsa_exception_fp_ieee_inexact 0
		.amdhsa_exception_int_div_zero 0
	.end_amdhsa_kernel

amdhsa.kernels:
  - .agpr_count:     0
    .args:
      - .actual_access:  read_only
        .address_space:  global
        .offset:         0
        .size:           8
        .value_kind:     global_buffer
      - .actual_access:  write_only
        .address_space:  global
        .offset:         8
        .size:           8
        .value_kind:     global_buffer
      - .offset:         16
        .size:           64
        .value_kind:     by_value
    .group_segment_fixed_size: 8224
    .kernarg_segment_align: 8
    .kernarg_segment_size: 80
    .language:       OpenCL C
    .language_version:
      - 2
      - 0
    .max_flat_workgroup_size: 256
    .name:           _Z9k1_streamPKfPf6PfArgs
    .private_segment_fixed_size: 0
    .sgpr_count:     28
    .sgpr_spill_count: 0
    .symbol:         _Z9k1_streamPKfPf6PfArgs.kd
    .uniform_work_group_size: 1
    .uses_dynamic_stack: false
    .vgpr_count:     72
    .vgpr_spill_count: 0
    .wavefront_size: 64
  - .agpr_count:     0
    .args:
      - .actual_access:  read_only
        .address_space:  global
        .offset:         0
        .size:           8
        .value_kind:     global_buffer
      - .actual_access:  read_only
        .address_space:  global
        .offset:         8
        .size:           8
        .value_kind:     global_buffer
      - .actual_access:  read_only
        .address_space:  global
        .offset:         16
        .size:           8
        .value_kind:     global_buffer
      - .actual_access:  write_only
        .address_space:  global
        .offset:         24
        .size:           8
        .value_kind:     global_buffer
      - .address_space:  global
        .offset:         32
        .size:           8
        .value_kind:     global_buffer
      - .address_space:  global
        .offset:         40
        .size:           8
        .value_kind:     global_buffer
    .group_segment_fixed_size: 3712
    .kernarg_segment_align: 8
    .kernarg_segment_size: 48
    .language:       OpenCL C
    .language_version:
      - 2
      - 0
    .max_flat_workgroup_size: 256
    .name:           _Z9k2_layer1PKfS0_S0_PfS1_S1_
    .private_segment_fixed_size: 0
    .sgpr_count:     32
    .sgpr_spill_count: 0
    .symbol:         _Z9k2_layer1PKfS0_S0_PfS1_S1_.kd
    .uniform_work_group_size: 1
    .uses_dynamic_stack: false
    .vgpr_count:     92
    .vgpr_spill_count: 0
    .wavefront_size: 64
  - .agpr_count:     8
    .args:
      - .actual_access:  read_only
        .address_space:  global
        .offset:         0
        .size:           8
        .value_kind:     global_buffer
      - .actual_access:  read_only
        .address_space:  global
        .offset:         8
        .size:           8
        .value_kind:     global_buffer
      - .actual_access:  read_only
        .address_space:  global
        .offset:         16
        .size:           8
        .value_kind:     global_buffer
      - .actual_access:  read_only
        .address_space:  global
        .offset:         24
        .size:           8
        .value_kind:     global_buffer
      - .actual_access:  read_only
        .address_space:  global
        .offset:         32
        .size:           8
        .value_kind:     global_buffer
      - .actual_access:  read_only
        .address_space:  global
        .offset:         40
        .size:           8
        .value_kind:     global_buffer
      - .actual_access:  read_only
        .address_space:  global
        .offset:         48
        .size:           8
        .value_kind:     global_buffer
      - .actual_access:  write_only
        .address_space:  global
        .offset:         56
        .size:           8
        .value_kind:     global_buffer
      - .address_space:  global
        .offset:         64
        .size:           8
        .value_kind:     global_buffer
      - .address_space:  global
        .offset:         72
        .size:           8
        .value_kind:     global_buffer
    .group_segment_fixed_size: 1280
    .kernarg_segment_align: 8
    .kernarg_segment_size: 80
    .language:       OpenCL C
    .language_version:
      - 2
      - 0
    .max_flat_workgroup_size: 256
    .name:           _Z7k_layerPKfS0_S0_S0_S0_S0_S0_PfS1_S1_
    .private_segment_fixed_size: 0
    .sgpr_count:     40
    .sgpr_spill_count: 0
    .symbol:         _Z7k_layerPKfS0_S0_S0_S0_S0_S0_PfS1_S1_.kd
    .uniform_work_group_size: 1
    .uses_dynamic_stack: false
    .vgpr_count:     104
    .vgpr_spill_count: 0
    .wavefront_size: 64
  - .agpr_count:     12
    .args:
      - .actual_access:  read_only
        .address_space:  global
        .offset:         0
        .size:           8
        .value_kind:     global_buffer
      - .actual_access:  read_only
        .address_space:  global
        .offset:         8
        .size:           8
        .value_kind:     global_buffer
      - .actual_access:  read_only
        .address_space:  global
        .offset:         16
        .size:           8
        .value_kind:     global_buffer
      - .actual_access:  read_only
        .address_space:  global
        .offset:         24
        .size:           8
        .value_kind:     global_buffer
      - .actual_access:  read_only
        .address_space:  global
        .offset:         32
        .size:           8
        .value_kind:     global_buffer
      - .actual_access:  read_only
        .address_space:  global
        .offset:         40
        .size:           8
        .value_kind:     global_buffer
      - .actual_access:  read_only
        .address_space:  global
        .offset:         48
        .size:           8
        .value_kind:     global_buffer
      - .actual_access:  read_only
        .address_space:  global
        .offset:         56
        .size:           8
        .value_kind:     global_buffer
      - .actual_access:  read_only
        .address_space:  global
        .offset:         64
        .size:           8
        .value_kind:     global_buffer
      - .actual_access:  write_only
        .address_space:  global
        .offset:         72
        .size:           8
        .value_kind:     global_buffer
    .group_segment_fixed_size: 4608
    .kernarg_segment_align: 8
    .kernarg_segment_size: 80
    .language:       OpenCL C
    .language_version:
      - 2
      - 0
    .max_flat_workgroup_size: 256
    .name:           _Z8k5_finalPKfS0_S0_S0_S0_S0_S0_S0_S0_Pf
    .private_segment_fixed_size: 0
    .sgpr_count:     30
    .sgpr_spill_count: 0
    .symbol:         _Z8k5_finalPKfS0_S0_S0_S0_S0_S0_S0_S0_Pf.kd
    .uniform_work_group_size: 1
    .uses_dynamic_stack: false
    .vgpr_count:     96
    .vgpr_spill_count: 0
    .wavefront_size: 64
